# s15p + rstd_fill (layer-0 PLE phase): 4 trips x 2 loads issued up front, math behind counted waits; padded
# speedup vs baseline: 1.0092x; 1.0047x over previous
; #define LAS __attribute__((address_space(3)))
; DI void rstd_fill(const Params& P, const Frame& F) {
;     const float* SS = (const float*)(P.ws + WS_T + T_SS); LAS float* rs = (LAS float*)(F.lds + LDS_RSTD); const int base = 2048 * (F.bid & 7);
;     for (int i = F.tid; i < 2048; i += NTHR) { const f32x4 a = *(const f32x4*)(SS + (size_t)(base + i) * 8), b = *(const f32x4*)(SS + (size_t)(base + i) * 8 + 4);
;         rs[i] = 1.0f / sqrtf((((a[0] + a[1]) + (a[2] + a[3])) + ((b[0] + b[1]) + (b[2] + b[3]))) * (1.0f / D) + EPS); }
;     __syncthreads();
.LBB0_1536:
	global_load_dwordx4 v[206:209], v[0:1], off
	global_load_dwordx4 v[210:213], v[0:1], off offset:16
	v_lshl_add_u64 v[0:1], v[0:1], 0, s[12:13]
	global_load_dwordx4 v[214:217], v[0:1], off
	global_load_dwordx4 v[218:221], v[0:1], off offset:16
	v_lshl_add_u64 v[0:1], v[0:1], 0, s[12:13]
	global_load_dwordx4 v[222:225], v[0:1], off
	global_load_dwordx4 v[226:229], v[0:1], off offset:16
	v_lshl_add_u64 v[0:1], v[0:1], 0, s[12:13]
	global_load_dwordx4 v[230:233], v[0:1], off
	global_load_dwordx4 v[234:237], v[0:1], off offset:16
	s_waitcnt vmcnt(6)
	v_mov_b32_e32 v6, v206
	v_mov_b32_e32 v7, v207
	v_mov_b32_e32 v8, v208
	v_mov_b32_e32 v9, v209
	v_mov_b32_e32 v10, v210
	v_mov_b32_e32 v11, v211
	v_mov_b32_e32 v12, v212
	v_mov_b32_e32 v13, v213
	v_mov_b32_e32 v14, v6
	v_mov_b32_e32 v15, v10
	v_mov_b32_e32 v10, v7
	v_mov_b32_e32 v6, v8
	v_mov_b32_e32 v7, v12
	v_mov_b32_e32 v12, v9
	v_pk_add_f32 v[8:9], v[14:15], v[10:11]
	v_pk_add_f32 v[6:7], v[6:7], v[12:13]
	s_nop 0
	v_pk_add_f32 v[6:7], v[8:9], v[6:7]
	s_nop 0
	v_add_f32_e32 v6, v6, v7
	v_fmamk_f32 v6, v6, 0x3a000000, v4
	v_mul_f32_e32 v7, 0x4f800000, v6
	v_cmp_gt_f32_e32 vcc, s9, v6
	s_nop 1
	v_cndmask_b32_e32 v6, v6, v7, vcc
	v_sqrt_f32_e32 v7, v6
	s_nop 0
	v_add_u32_e32 v8, -1, v7
	v_add_u32_e32 v9, 1, v7
	v_fma_f32 v10, -v8, v7, v6
	v_fma_f32 v11, -v9, v7, v6
	v_cmp_ge_f32_e64 s[4:5], 0, v10
	s_nop 1
	v_cndmask_b32_e64 v7, v7, v8, s[4:5]
	v_cmp_lt_f32_e64 s[4:5], 0, v11
	s_nop 1
	v_cndmask_b32_e64 v7, v7, v9, s[4:5]
	v_mul_f32_e32 v8, 0x37800000, v7
	v_cndmask_b32_e32 v7, v7, v8, vcc
	v_cmp_class_f32_e32 vcc, v6, v5
	s_nop 1
	v_cndmask_b32_e32 v6, v7, v6, vcc
	v_div_scale_f32 v7, s[4:5], v6, v6, 1.0
	v_rcp_f32_e32 v8, v7
	v_div_scale_f32 v9, vcc, 1.0, v6, 1.0
	v_fma_f32 v10, -v7, v8, 1.0
	v_fmac_f32_e32 v8, v10, v8
	v_mul_f32_e32 v10, v9, v8
	v_fma_f32 v11, -v7, v10, v9
	v_fmac_f32_e32 v10, v11, v8
	v_fma_f32 v7, -v7, v10, v9
	v_div_fmas_f32 v7, v7, v8, v10
	v_div_fixup_f32 v6, v7, v6, 1.0
	ds_write_b32 v3, v6
	v_add_u32_e32 v3, 0x800, v3
	s_waitcnt vmcnt(4)
	v_mov_b32_e32 v6, v214
	v_mov_b32_e32 v7, v215
	v_mov_b32_e32 v8, v216
	v_mov_b32_e32 v9, v217
	v_mov_b32_e32 v10, v218
	v_mov_b32_e32 v11, v219
	v_mov_b32_e32 v12, v220
	v_mov_b32_e32 v13, v221
	v_mov_b32_e32 v14, v6
	v_mov_b32_e32 v15, v10
	v_mov_b32_e32 v10, v7
	v_mov_b32_e32 v6, v8
	v_mov_b32_e32 v7, v12
	v_mov_b32_e32 v12, v9
	v_pk_add_f32 v[8:9], v[14:15], v[10:11]
	v_pk_add_f32 v[6:7], v[6:7], v[12:13]
	s_nop 0
	v_pk_add_f32 v[6:7], v[8:9], v[6:7]
	s_nop 0
	v_add_f32_e32 v6, v6, v7
	v_fmamk_f32 v6, v6, 0x3a000000, v4
	v_mul_f32_e32 v7, 0x4f800000, v6
	v_cmp_gt_f32_e32 vcc, s9, v6
	s_nop 1
	v_cndmask_b32_e32 v6, v6, v7, vcc
	v_sqrt_f32_e32 v7, v6
	s_nop 0
	v_add_u32_e32 v8, -1, v7
	v_add_u32_e32 v9, 1, v7
	v_fma_f32 v10, -v8, v7, v6
	v_fma_f32 v11, -v9, v7, v6
	v_cmp_ge_f32_e64 s[4:5], 0, v10
	s_nop 1
	v_cndmask_b32_e64 v7, v7, v8, s[4:5]
	v_cmp_lt_f32_e64 s[4:5], 0, v11
	s_nop 1
	v_cndmask_b32_e64 v7, v7, v9, s[4:5]
	v_mul_f32_e32 v8, 0x37800000, v7
	v_cndmask_b32_e32 v7, v7, v8, vcc
	v_cmp_class_f32_e32 vcc, v6, v5
	s_nop 1
	v_cndmask_b32_e32 v6, v7, v6, vcc
	v_div_scale_f32 v7, s[4:5], v6, v6, 1.0
	v_rcp_f32_e32 v8, v7
	v_div_scale_f32 v9, vcc, 1.0, v6, 1.0
	v_fma_f32 v10, -v7, v8, 1.0
	v_fmac_f32_e32 v8, v10, v8
	v_mul_f32_e32 v10, v9, v8
	v_fma_f32 v11, -v7, v10, v9
	v_fmac_f32_e32 v10, v11, v8
	v_fma_f32 v7, -v7, v10, v9
	v_div_fmas_f32 v7, v7, v8, v10
	v_div_fixup_f32 v6, v7, v6, 1.0
	ds_write_b32 v3, v6
	v_add_u32_e32 v3, 0x800, v3
	s_waitcnt vmcnt(2)
	v_mov_b32_e32 v6, v222
	v_mov_b32_e32 v7, v223
	v_mov_b32_e32 v8, v224
	v_mov_b32_e32 v9, v225
	v_mov_b32_e32 v10, v226
	v_mov_b32_e32 v11, v227
	v_mov_b32_e32 v12, v228
	v_mov_b32_e32 v13, v229
	v_mov_b32_e32 v14, v6
	v_mov_b32_e32 v15, v10
	v_mov_b32_e32 v10, v7
	v_mov_b32_e32 v6, v8
	v_mov_b32_e32 v7, v12
	v_mov_b32_e32 v12, v9
	v_pk_add_f32 v[8:9], v[14:15], v[10:11]
	v_pk_add_f32 v[6:7], v[6:7], v[12:13]
	s_nop 0
	v_pk_add_f32 v[6:7], v[8:9], v[6:7]
	s_nop 0
	v_add_f32_e32 v6, v6, v7
	v_fmamk_f32 v6, v6, 0x3a000000, v4
	v_mul_f32_e32 v7, 0x4f800000, v6
	v_cmp_gt_f32_e32 vcc, s9, v6
	s_nop 1
	v_cndmask_b32_e32 v6, v6, v7, vcc
	v_sqrt_f32_e32 v7, v6
	s_nop 0
	v_add_u32_e32 v8, -1, v7
	v_add_u32_e32 v9, 1, v7
	v_fma_f32 v10, -v8, v7, v6
	v_fma_f32 v11, -v9, v7, v6
	v_cmp_ge_f32_e64 s[4:5], 0, v10
	s_nop 1
	v_cndmask_b32_e64 v7, v7, v8, s[4:5]
	v_cmp_lt_f32_e64 s[4:5], 0, v11
	s_nop 1
	v_cndmask_b32_e64 v7, v7, v9, s[4:5]
	v_mul_f32_e32 v8, 0x37800000, v7
	v_cndmask_b32_e32 v7, v7, v8, vcc
	v_cmp_class_f32_e32 vcc, v6, v5
	s_nop 1
	v_cndmask_b32_e32 v6, v7, v6, vcc
	v_div_scale_f32 v7, s[4:5], v6, v6, 1.0
	v_rcp_f32_e32 v8, v7
	v_div_scale_f32 v9, vcc, 1.0, v6, 1.0
	v_fma_f32 v10, -v7, v8, 1.0
	v_fmac_f32_e32 v8, v10, v8
	v_mul_f32_e32 v10, v9, v8
	v_fma_f32 v11, -v7, v10, v9
	v_fmac_f32_e32 v10, v11, v8
	v_fma_f32 v7, -v7, v10, v9
	v_div_fmas_f32 v7, v7, v8, v10
	v_div_fixup_f32 v6, v7, v6, 1.0
	ds_write_b32 v3, v6
	v_add_u32_e32 v3, 0x800, v3
	s_waitcnt vmcnt(0)
	v_mov_b32_e32 v6, v230
	v_mov_b32_e32 v7, v231
	v_mov_b32_e32 v8, v232
	v_mov_b32_e32 v9, v233
	v_mov_b32_e32 v10, v234
	v_mov_b32_e32 v11, v235
	v_mov_b32_e32 v12, v236
	v_mov_b32_e32 v13, v237
	v_mov_b32_e32 v14, v6
	v_mov_b32_e32 v15, v10
	v_mov_b32_e32 v10, v7
	v_mov_b32_e32 v6, v8
	v_mov_b32_e32 v7, v12
	v_mov_b32_e32 v12, v9
	v_pk_add_f32 v[8:9], v[14:15], v[10:11]
	v_pk_add_f32 v[6:7], v[6:7], v[12:13]
	s_nop 0
	v_pk_add_f32 v[6:7], v[8:9], v[6:7]
	s_nop 0
	v_add_f32_e32 v6, v6, v7
	v_fmamk_f32 v6, v6, 0x3a000000, v4
	v_mul_f32_e32 v7, 0x4f800000, v6
	v_cmp_gt_f32_e32 vcc, s9, v6
	s_nop 1
	v_cndmask_b32_e32 v6, v6, v7, vcc
	v_sqrt_f32_e32 v7, v6
	s_nop 0
	v_add_u32_e32 v8, -1, v7
	v_add_u32_e32 v9, 1, v7
	v_fma_f32 v10, -v8, v7, v6
	v_fma_f32 v11, -v9, v7, v6
	v_cmp_ge_f32_e64 s[4:5], 0, v10
	s_nop 1
	v_cndmask_b32_e64 v7, v7, v8, s[4:5]
	v_cmp_lt_f32_e64 s[4:5], 0, v11
	s_nop 1
	v_cndmask_b32_e64 v7, v7, v9, s[4:5]
	v_mul_f32_e32 v8, 0x37800000, v7
	v_cndmask_b32_e32 v7, v7, v8, vcc
	v_cmp_class_f32_e32 vcc, v6, v5
	s_nop 1
	v_cndmask_b32_e32 v6, v7, v6, vcc
	v_div_scale_f32 v7, s[4:5], v6, v6, 1.0
	v_rcp_f32_e32 v8, v7
	v_div_scale_f32 v9, vcc, 1.0, v6, 1.0
	v_fma_f32 v10, -v7, v8, 1.0
	v_fmac_f32_e32 v8, v10, v8
	v_mul_f32_e32 v10, v9, v8
	v_fma_f32 v11, -v7, v10, v9
	v_fmac_f32_e32 v10, v11, v8
	v_fma_f32 v7, -v7, v10, v9
	v_div_fmas_f32 v7, v7, v8, v10
	v_div_fixup_f32 v6, v7, v6, 1.0
	ds_write_b32 v3, v6
	v_add_u32_e32 v3, 0x800, v3
	v_lshl_add_u64 v[0:1], v[0:1], 0, s[12:13]
	v_add_u32_e32 v2, 0x800, v2
	s_mov_b64 s[10:11], exec
